# conversion routine tile loads use system-scope streaming policy (sc0 sc1 nt) to keep them out of the caches the concurrent GEMM workgroups use
# speedup vs baseline: 1.0059x; 1.0059x over previous
; #define SB() __builtin_amdgcn_sched_barrier(0)
; __device__ __forceinline__ void wg_convert_tile(Frame& F, const float* W, int ldw, bf16_t* WT, int Kd, int k0, int n0, int kind, const float* kgain) {
;     ...
;     f32x4 ld[2][8];
; #pragma unroll
;     for (int j = 0; j < 8; ++j) ld[0][j] = __builtin_nontemporal_load((const f32x4*)(src + (size_t)j * ldw));
; #pragma unroll
;     for (int p = 0; p < 4; ++p) {
;         if (p < 3) {
; #pragma unroll
;             for (int j = 0; j < 8; ++j) ld[(p + 1) & 1][j] = __builtin_nontemporal_load((const f32x4*)(src + (size_t)(64 * (p + 1) + j) * ldw)); }
;         float g[8];
; #pragma unroll
;         for (int j = 0; j < 8; ++j) g[j] = kgain ? kgain[k0 + 64 * p + 8 * w + j] : 1.f;
;         SB();
.Lcv_nogain:
	s_barrier
	s_mov_b64 s[80:81], s[38:39]
	s_mul_i32 s98, s32, 56
	global_load_dwordx4 v[96:99], v3, s[80:81] sc0 sc1 nt
	s_add_u32 s80, s80, s32
	s_addc_u32 s81, s81, 0
	global_load_dwordx4 v[100:103], v3, s[80:81] sc0 sc1 nt
	s_add_u32 s80, s80, s32
	s_addc_u32 s81, s81, 0
	global_load_dwordx4 v[104:107], v3, s[80:81] sc0 sc1 nt
	s_add_u32 s80, s80, s32
	s_addc_u32 s81, s81, 0
	global_load_dwordx4 v[108:111], v3, s[80:81] sc0 sc1 nt
	s_add_u32 s80, s80, s32
	s_addc_u32 s81, s81, 0
	global_load_dwordx4 v[112:115], v3, s[80:81] sc0 sc1 nt
	s_add_u32 s80, s80, s32
	s_addc_u32 s81, s81, 0
	global_load_dwordx4 v[116:119], v3, s[80:81] sc0 sc1 nt
	s_add_u32 s80, s80, s32
	s_addc_u32 s81, s81, 0
	global_load_dwordx4 v[120:123], v3, s[80:81] sc0 sc1 nt
	s_add_u32 s80, s80, s32
	s_addc_u32 s81, s81, 0
	global_load_dwordx4 v[124:127], v3, s[80:81] sc0 sc1 nt
	s_add_u32 s80, s80, s32
	s_addc_u32 s81, s81, 0
	s_add_u32 s80, s80, s98
	s_addc_u32 s81, s81, 0
	global_load_dwordx4 v[128:131], v3, s[80:81] sc0 sc1 nt
	s_add_u32 s80, s80, s32
	s_addc_u32 s81, s81, 0
	global_load_dwordx4 v[132:135], v3, s[80:81] sc0 sc1 nt
	s_add_u32 s80, s80, s32
	s_addc_u32 s81, s81, 0
	global_load_dwordx4 v[136:139], v3, s[80:81] sc0 sc1 nt
	s_add_u32 s80, s80, s32
	s_addc_u32 s81, s81, 0
	global_load_dwordx4 v[140:143], v3, s[80:81] sc0 sc1 nt
	s_add_u32 s80, s80, s32
	s_addc_u32 s81, s81, 0
	global_load_dwordx4 v[144:147], v3, s[80:81] sc0 sc1 nt
	s_add_u32 s80, s80, s32
	s_addc_u32 s81, s81, 0
	global_load_dwordx4 v[148:151], v3, s[80:81] sc0 sc1 nt
	s_add_u32 s80, s80, s32
	s_addc_u32 s81, s81, 0
	global_load_dwordx4 v[152:155], v3, s[80:81] sc0 sc1 nt
	s_add_u32 s80, s80, s32
	s_addc_u32 s81, s81, 0
	global_load_dwordx4 v[156:159], v3, s[80:81] sc0 sc1 nt
	s_add_u32 s80, s80, s32
	s_addc_u32 s81, s81, 0
	s_add_u32 s80, s80, s98
	s_addc_u32 s81, s81, 0
	global_load_dwordx4 v[160:163], v3, s[80:81] sc0 sc1 nt
	s_add_u32 s80, s80, s32
	s_addc_u32 s81, s81, 0
	global_load_dwordx4 v[164:167], v3, s[80:81] sc0 sc1 nt
	s_add_u32 s80, s80, s32
	s_addc_u32 s81, s81, 0
	global_load_dwordx4 v[168:171], v3, s[80:81] sc0 sc1 nt
	s_add_u32 s80, s80, s32
	s_addc_u32 s81, s81, 0
	global_load_dwordx4 v[172:175], v3, s[80:81] sc0 sc1 nt
	s_add_u32 s80, s80, s32
	s_addc_u32 s81, s81, 0
	global_load_dwordx4 v[176:179], v3, s[80:81] sc0 sc1 nt
	s_add_u32 s80, s80, s32
	s_addc_u32 s81, s81, 0
	global_load_dwordx4 v[180:183], v3, s[80:81] sc0 sc1 nt
	s_add_u32 s80, s80, s32
	s_addc_u32 s81, s81, 0
	global_load_dwordx4 v[184:187], v3, s[80:81] sc0 sc1 nt
	s_add_u32 s80, s80, s32
	s_addc_u32 s81, s81, 0
	global_load_dwordx4 v[188:191], v3, s[80:81] sc0 sc1 nt
	s_add_u32 s80, s80, s32
	s_addc_u32 s81, s81, 0
	s_add_u32 s80, s80, s98
	s_addc_u32 s81, s81, 0
	global_load_dwordx4 v[192:195], v3, s[80:81] sc0 sc1 nt
	s_add_u32 s80, s80, s32
	s_addc_u32 s81, s81, 0
	global_load_dwordx4 v[196:199], v3, s[80:81] sc0 sc1 nt
	s_add_u32 s80, s80, s32
	s_addc_u32 s81, s81, 0
	global_load_dwordx4 v[200:203], v3, s[80:81] sc0 sc1 nt
	s_add_u32 s80, s80, s32
	s_addc_u32 s81, s81, 0
	global_load_dwordx4 v[204:207], v3, s[80:81] sc0 sc1 nt
	s_add_u32 s80, s80, s32
	s_addc_u32 s81, s81, 0
	global_load_dwordx4 v[208:211], v3, s[80:81] sc0 sc1 nt
	s_add_u32 s80, s80, s32
	s_addc_u32 s81, s81, 0
	global_load_dwordx4 v[212:215], v3, s[80:81] sc0 sc1 nt
	s_add_u32 s80, s80, s32
	s_addc_u32 s81, s81, 0
	global_load_dwordx4 v[20:23], v3, s[80:81] sc0 sc1 nt
	s_add_u32 s80, s80, s32
	s_addc_u32 s81, s81, 0
	global_load_dwordx4 v[24:27], v3, s[80:81] sc0 sc1 nt
	s_waitcnt vmcnt(24)
	s_add_i32 s99, s8, 0
	v_xor_b32_e32 v5, s99, v14
	v_lshlrev_b32_e32 v5, 4, v5
	v_lshl_add_u32 v5, v2, 11, v5
	v_mul_f32_e32 v12, v28, v96
	v_mul_f32_e32 v13, v29, v100
	v_cvt_pk_bf16_f32 v8, v12, v13
	v_mul_f32_e32 v12, v30, v104
	v_mul_f32_e32 v13, v31, v108
	v_cvt_pk_bf16_f32 v9, v12, v13
	v_mul_f32_e32 v12, v32, v112
	v_mul_f32_e32 v13, v33, v116
	v_cvt_pk_bf16_f32 v10, v12, v13
	v_mul_f32_e32 v12, v34, v120
	v_mul_f32_e32 v13, v35, v124
	v_cvt_pk_bf16_f32 v11, v12, v13
	ds_write_b128 v5, v[8:11]
	v_mul_f32_e32 v12, v28, v97
	v_mul_f32_e32 v13, v29, v101
	v_cvt_pk_bf16_f32 v8, v12, v13
	v_mul_f32_e32 v12, v30, v105
	v_mul_f32_e32 v13, v31, v109
	v_cvt_pk_bf16_f32 v9, v12, v13
	v_mul_f32_e32 v12, v32, v113
	v_mul_f32_e32 v13, v33, v117
	v_cvt_pk_bf16_f32 v10, v12, v13
	v_mul_f32_e32 v12, v34, v121
	v_mul_f32_e32 v13, v35, v125
	v_cvt_pk_bf16_f32 v11, v12, v13
	ds_write_b128 v5, v[8:11] offset:512
	v_mul_f32_e32 v12, v28, v98
	v_mul_f32_e32 v13, v29, v102
	v_cvt_pk_bf16_f32 v8, v12, v13
	v_mul_f32_e32 v12, v30, v106
	v_mul_f32_e32 v13, v31, v110
	v_cvt_pk_bf16_f32 v9, v12, v13
	v_mul_f32_e32 v12, v32, v114
	v_mul_f32_e32 v13, v33, v118
	v_cvt_pk_bf16_f32 v10, v12, v13
	v_mul_f32_e32 v12, v34, v122
	v_mul_f32_e32 v13, v35, v126
	v_cvt_pk_bf16_f32 v11, v12, v13
	ds_write_b128 v5, v[8:11] offset:1024
	v_mul_f32_e32 v12, v28, v99
	v_mul_f32_e32 v13, v29, v103
	v_cvt_pk_bf16_f32 v8, v12, v13
	v_mul_f32_e32 v12, v30, v107
	v_mul_f32_e32 v13, v31, v111
	v_cvt_pk_bf16_f32 v9, v12, v13
	v_mul_f32_e32 v12, v32, v115
	v_mul_f32_e32 v13, v33, v119
	v_cvt_pk_bf16_f32 v10, v12, v13
	v_mul_f32_e32 v12, v34, v123
	v_mul_f32_e32 v13, v35, v127
	v_cvt_pk_bf16_f32 v11, v12, v13
	ds_write_b128 v5, v[8:11] offset:1536
	s_waitcnt vmcnt(16)
; #define LAS __attribute__((address_space(3)))
; #define SB() __builtin_amdgcn_sched_barrier(0)
; __device__ __forceinline__ unsigned cvt_pk_bf16(float lo, float hi) { unsigned r; asm volatile("v_cvt_pk_bf16_f32 %0, %1, %2" : "=v"(r) : "v"(lo), "v"(hi)); return r; }
; __device__ __forceinline__ void wg_convert_tile(Frame& F, const float* W, int ldw, bf16_t* WT, int Kd, int k0, int n0, int kind, const float* kgain) {
;     ...
; #pragma unroll
;     for (int p = 0; p < 4; ++p) {
;         if (p < 3) {
; #pragma unroll
;             for (int j = 0; j < 8; ++j) ld[(p + 1) & 1][j] = __builtin_nontemporal_load((const f32x4*)(src + (size_t)(64 * (p + 1) + j) * ldw)); }
;         float g[8];
; #pragma unroll
;         for (int j = 0; j < 8; ++j) g[j] = kgain ? kgain[k0 + 64 * p + 8 * w + j] : 1.f;
;         SB();
;         const unsigned kc = (unsigned)(8 * p + w);
; #pragma unroll
;         for (int c = 0; c < 4; ++c) { const int n = 4 * lane + c;
;             u32x4 o; o.x = cvt_pk_bf16(ld[p & 1][0][c] * g[0], ld[p & 1][1][c] * g[1]); o.y = cvt_pk_bf16(ld[p & 1][2][c] * g[2], ld[p & 1][3][c] * g[3]);
;                      o.z = cvt_pk_bf16(ld[p & 1][4][c] * g[4], ld[p & 1][5][c] * g[5]); o.w = cvt_pk_bf16(ld[p & 1][6][c] * g[6], ld[p & 1][7][c] * g[7]);
;             *(LAS u32x4*)(img + n * 512 + ((kc ^ (unsigned)(lane & 31)) << 4)) = o; }
;         SB();
;     }
	s_add_i32 s99, s8, 8
	v_xor_b32_e32 v5, s99, v14
	v_lshlrev_b32_e32 v5, 4, v5
	v_lshl_add_u32 v5, v2, 11, v5
	v_mul_f32_e32 v12, v36, v128
	v_mul_f32_e32 v13, v37, v132
	v_cvt_pk_bf16_f32 v8, v12, v13
	v_mul_f32_e32 v12, v38, v136
	v_mul_f32_e32 v13, v39, v140
	v_cvt_pk_bf16_f32 v9, v12, v13
	v_mul_f32_e32 v12, v40, v144
	v_mul_f32_e32 v13, v41, v148
	v_cvt_pk_bf16_f32 v10, v12, v13
	v_mul_f32_e32 v12, v42, v152
	v_mul_f32_e32 v13, v43, v156
	v_cvt_pk_bf16_f32 v11, v12, v13
	ds_write_b128 v5, v[8:11]
	v_mul_f32_e32 v12, v36, v129
	v_mul_f32_e32 v13, v37, v133
	v_cvt_pk_bf16_f32 v8, v12, v13
	v_mul_f32_e32 v12, v38, v137
	v_mul_f32_e32 v13, v39, v141
	v_cvt_pk_bf16_f32 v9, v12, v13
	v_mul_f32_e32 v12, v40, v145
	v_mul_f32_e32 v13, v41, v149
	v_cvt_pk_bf16_f32 v10, v12, v13
	v_mul_f32_e32 v12, v42, v153
	v_mul_f32_e32 v13, v43, v157
	v_cvt_pk_bf16_f32 v11, v12, v13
	ds_write_b128 v5, v[8:11] offset:512
	v_mul_f32_e32 v12, v36, v130
	v_mul_f32_e32 v13, v37, v134
	v_cvt_pk_bf16_f32 v8, v12, v13
	v_mul_f32_e32 v12, v38, v138
	v_mul_f32_e32 v13, v39, v142
	v_cvt_pk_bf16_f32 v9, v12, v13
	v_mul_f32_e32 v12, v40, v146
	v_mul_f32_e32 v13, v41, v150
	v_cvt_pk_bf16_f32 v10, v12, v13
	v_mul_f32_e32 v12, v42, v154
	v_mul_f32_e32 v13, v43, v158
	v_cvt_pk_bf16_f32 v11, v12, v13
	ds_write_b128 v5, v[8:11] offset:1024
	v_mul_f32_e32 v12, v36, v131
	v_mul_f32_e32 v13, v37, v135
	v_cvt_pk_bf16_f32 v8, v12, v13
	v_mul_f32_e32 v12, v38, v139
	v_mul_f32_e32 v13, v39, v143
	v_cvt_pk_bf16_f32 v9, v12, v13
	v_mul_f32_e32 v12, v40, v147
	v_mul_f32_e32 v13, v41, v151
	v_cvt_pk_bf16_f32 v10, v12, v13
	v_mul_f32_e32 v12, v42, v155
	v_mul_f32_e32 v13, v43, v159
	v_cvt_pk_bf16_f32 v11, v12, v13
	ds_write_b128 v5, v[8:11] offset:1536
	s_waitcnt vmcnt(8)
	s_add_i32 s99, s8, 16
	v_xor_b32_e32 v5, s99, v14
	v_lshlrev_b32_e32 v5, 4, v5
	v_lshl_add_u32 v5, v2, 11, v5
	v_mul_f32_e32 v12, v44, v160
	v_mul_f32_e32 v13, v45, v164
	v_cvt_pk_bf16_f32 v8, v12, v13
	v_mul_f32_e32 v12, v46, v168
	v_mul_f32_e32 v13, v47, v172
	v_cvt_pk_bf16_f32 v9, v12, v13
	v_mul_f32_e32 v12, v50, v176
	v_mul_f32_e32 v13, v51, v180
	v_cvt_pk_bf16_f32 v10, v12, v13
	v_mul_f32_e32 v12, v52, v184
	v_mul_f32_e32 v13, v53, v188
	v_cvt_pk_bf16_f32 v11, v12, v13
	ds_write_b128 v5, v[8:11]
	v_mul_f32_e32 v12, v44, v161
	v_mul_f32_e32 v13, v45, v165
	v_cvt_pk_bf16_f32 v8, v12, v13
	v_mul_f32_e32 v12, v46, v169
	v_mul_f32_e32 v13, v47, v173
	v_cvt_pk_bf16_f32 v9, v12, v13
	v_mul_f32_e32 v12, v50, v177
	v_mul_f32_e32 v13, v51, v181
	v_cvt_pk_bf16_f32 v10, v12, v13
	v_mul_f32_e32 v12, v52, v185
	v_mul_f32_e32 v13, v53, v189
	v_cvt_pk_bf16_f32 v11, v12, v13
	ds_write_b128 v5, v[8:11] offset:512
	v_mul_f32_e32 v12, v44, v162
	v_mul_f32_e32 v13, v45, v166
	v_cvt_pk_bf16_f32 v8, v12, v13
	v_mul_f32_e32 v12, v46, v170
	v_mul_f32_e32 v13, v47, v174
	v_cvt_pk_bf16_f32 v9, v12, v13
	v_mul_f32_e32 v12, v50, v178
	v_mul_f32_e32 v13, v51, v182
	v_cvt_pk_bf16_f32 v10, v12, v13
	v_mul_f32_e32 v12, v52, v186
	v_mul_f32_e32 v13, v53, v190
	v_cvt_pk_bf16_f32 v11, v12, v13
	ds_write_b128 v5, v[8:11] offset:1024
	v_mul_f32_e32 v12, v44, v163
	v_mul_f32_e32 v13, v45, v167
	v_cvt_pk_bf16_f32 v8, v12, v13
	v_mul_f32_e32 v12, v46, v171
	v_mul_f32_e32 v13, v47, v175
	v_cvt_pk_bf16_f32 v9, v12, v13
	v_mul_f32_e32 v12, v50, v179
	v_mul_f32_e32 v13, v51, v183
	v_cvt_pk_bf16_f32 v10, v12, v13
	v_mul_f32_e32 v12, v52, v187
	v_mul_f32_e32 v13, v53, v191
	v_cvt_pk_bf16_f32 v11, v12, v13
	ds_write_b128 v5, v[8:11] offset:1536
	s_waitcnt vmcnt(0)
	s_add_i32 s99, s8, 24
	v_xor_b32_e32 v5, s99, v14
	v_lshlrev_b32_e32 v5, 4, v5
	v_lshl_add_u32 v5, v2, 11, v5
	v_mul_f32_e32 v12, v54, v192
	v_mul_f32_e32 v13, v55, v196
	v_cvt_pk_bf16_f32 v8, v12, v13
	v_mul_f32_e32 v12, v56, v200
	v_mul_f32_e32 v13, v57, v204
	v_cvt_pk_bf16_f32 v9, v12, v13
	v_mul_f32_e32 v12, v58, v208
	v_mul_f32_e32 v13, v59, v212
	v_cvt_pk_bf16_f32 v10, v12, v13
	v_mul_f32_e32 v12, v60, v20
	v_mul_f32_e32 v13, v61, v24
	v_cvt_pk_bf16_f32 v11, v12, v13
	ds_write_b128 v5, v[8:11]
	v_mul_f32_e32 v12, v54, v193
	v_mul_f32_e32 v13, v55, v197
	v_cvt_pk_bf16_f32 v8, v12, v13
	v_mul_f32_e32 v12, v56, v201
	v_mul_f32_e32 v13, v57, v205
	v_cvt_pk_bf16_f32 v9, v12, v13
	v_mul_f32_e32 v12, v58, v209
	v_mul_f32_e32 v13, v59, v213
	v_cvt_pk_bf16_f32 v10, v12, v13
	v_mul_f32_e32 v12, v60, v21
	v_mul_f32_e32 v13, v61, v25
	v_cvt_pk_bf16_f32 v11, v12, v13
	ds_write_b128 v5, v[8:11] offset:512
	v_mul_f32_e32 v12, v54, v194
	v_mul_f32_e32 v13, v55, v198
	v_cvt_pk_bf16_f32 v8, v12, v13
	v_mul_f32_e32 v12, v56, v202
	v_mul_f32_e32 v13, v57, v206
	v_cvt_pk_bf16_f32 v9, v12, v13
	v_mul_f32_e32 v12, v58, v210
	v_mul_f32_e32 v13, v59, v214
	v_cvt_pk_bf16_f32 v10, v12, v13
	v_mul_f32_e32 v12, v60, v22
	v_mul_f32_e32 v13, v61, v26
	v_cvt_pk_bf16_f32 v11, v12, v13
	ds_write_b128 v5, v[8:11] offset:1024
	v_mul_f32_e32 v12, v54, v195
	v_mul_f32_e32 v13, v55, v199
	v_cvt_pk_bf16_f32 v8, v12, v13
	v_mul_f32_e32 v12, v56, v203
	v_mul_f32_e32 v13, v57, v207
	v_cvt_pk_bf16_f32 v9, v12, v13
	v_mul_f32_e32 v12, v58, v211
	v_mul_f32_e32 v13, v59, v215
	v_cvt_pk_bf16_f32 v10, v12, v13
	v_mul_f32_e32 v12, v60, v23
	v_mul_f32_e32 v13, v61, v27
	v_cvt_pk_bf16_f32 v11, v12, v13
	ds_write_b128 v5, v[8:11] offset:1536
	s_waitcnt lgkmcnt(0)
	s_barrier
; #define LAS __attribute__((address_space(3)))
; #define GAS __attribute__((address_space(1)))
; #define SB() __builtin_amdgcn_sched_barrier(0)
; #define LDS_WAIT() asm volatile("s_waitcnt lgkmcnt(0)" ::: "memory")
; __device__ __forceinline__ void wg_convert_tile(Frame& F, const float* W, int ldw, bf16_t* WT, int Kd, int k0, int n0, int kind, const float* kgain) {
;     ...
;     LDS_WAIT(); __syncthreads();
; #pragma unroll
;     for (int t = 0; t < 16; t += 4) { u32x4 v[4];
; #pragma unroll
;         for (int q = 0; q < 4; ++q) { const int idx = (t + q) * 512 + w * 64 + lane, n = idx >> 5, kc = idx & 31; v[q] = *(const LAS u32x4*)(img + n * 512 + ((kc ^ ((n >> 2) & 31)) << 4)); }
;         SB();
; #pragma unroll
;         for (int q = 0; q < 4; ++q) { const int idx = (t + q) * 512 + w * 64 + lane, n = idx >> 5, kc = idx & 31, nn = n0 + n;
;             const int row = kind < 0 ? nn : ((nn >> 7) * 256 + kind * 128 + (nn & 127));
;             __builtin_nontemporal_store(v[q], (GAS u32x4*)(WT + (size_t)row * Kd + k0 + 8 * kc)); }
;         SB(); }
;     LDS_WAIT(); __syncthreads();
	v_lshlrev_b32_e32 v18, 9, v16
	s_lshr_b32 s83, s8, 1
	s_add_i32 s98, s83, 0
	s_and_b32 s98, s98, 31
	v_xor_b32_e32 v7, s98, v14
	v_lshlrev_b32_e32 v7, 4, v7
	s_mov_b32 s99, 0
	v_add3_u32 v7, v7, v18, s99
	ds_read_b128 v[96:99], v7
	s_add_i32 s98, s83, 4
	s_and_b32 s98, s98, 31
	v_xor_b32_e32 v7, s98, v14
	v_lshlrev_b32_e32 v7, 4, v7
	s_mov_b32 s99, 8192
	v_add3_u32 v7, v7, v18, s99
	ds_read_b128 v[100:103], v7
	s_add_i32 s98, s83, 8
	s_and_b32 s98, s98, 31
	v_xor_b32_e32 v7, s98, v14
	v_lshlrev_b32_e32 v7, 4, v7
	s_mov_b32 s99, 16384
	v_add3_u32 v7, v7, v18, s99
	ds_read_b128 v[104:107], v7
	s_add_i32 s98, s83, 12
	s_and_b32 s98, s98, 31
	v_xor_b32_e32 v7, s98, v14
	v_lshlrev_b32_e32 v7, 4, v7
	s_mov_b32 s99, 24576
	v_add3_u32 v7, v7, v18, s99
	ds_read_b128 v[108:111], v7
	s_waitcnt lgkmcnt(0)
	s_movk_i32 s98, 0
	s_mul_i32 s98, s98, s55
	s_add_u32 s98, s64, s98
	s_addc_u32 s99, s65, 0
	global_store_dwordx4 v6, v[96:99], s[98:99] nt
	s_movk_i32 s98, 16
	s_mul_i32 s98, s98, s55
	s_add_u32 s98, s64, s98
	s_addc_u32 s99, s65, 0
	global_store_dwordx4 v6, v[100:103], s[98:99] nt
	s_movk_i32 s98, 32
	s_mul_i32 s98, s98, s55
	s_add_u32 s98, s64, s98
	s_addc_u32 s99, s65, 0
	global_store_dwordx4 v6, v[104:107], s[98:99] nt
	s_movk_i32 s98, 48
	s_mul_i32 s98, s98, s55
	s_add_u32 s98, s64, s98
	s_addc_u32 s99, s65, 0
	global_store_dwordx4 v6, v[108:111], s[98:99] nt
	s_add_i32 s98, s83, 16
	s_and_b32 s98, s98, 31
	v_xor_b32_e32 v7, s98, v14
	v_lshlrev_b32_e32 v7, 4, v7
	s_mov_b32 s99, 32768
	v_add3_u32 v7, v7, v18, s99
	ds_read_b128 v[96:99], v7
	s_add_i32 s98, s83, 20
	s_and_b32 s98, s98, 31
	v_xor_b32_e32 v7, s98, v14
	v_lshlrev_b32_e32 v7, 4, v7
	s_mov_b32 s99, 40960
	v_add3_u32 v7, v7, v18, s99
	ds_read_b128 v[100:103], v7
	s_add_i32 s98, s83, 24
	s_and_b32 s98, s98, 31
	v_xor_b32_e32 v7, s98, v14
	v_lshlrev_b32_e32 v7, 4, v7
	s_mov_b32 s99, 49152
	v_add3_u32 v7, v7, v18, s99
	ds_read_b128 v[104:107], v7
	s_add_i32 s98, s83, 28
	s_and_b32 s98, s98, 31
	v_xor_b32_e32 v7, s98, v14
	v_lshlrev_b32_e32 v7, 4, v7
	s_mov_b32 s99, 57344
	v_add3_u32 v7, v7, v18, s99
	ds_read_b128 v[108:111], v7
	s_waitcnt lgkmcnt(0)
	s_movk_i32 s98, 64
	s_mul_i32 s98, s98, s55
	s_add_u32 s98, s64, s98
	s_addc_u32 s99, s65, 0
	global_store_dwordx4 v6, v[96:99], s[98:99] nt
	s_movk_i32 s98, 80
	s_mul_i32 s98, s98, s55
	s_add_u32 s98, s64, s98
	s_addc_u32 s99, s65, 0
	global_store_dwordx4 v6, v[100:103], s[98:99] nt
	s_movk_i32 s98, 96
	s_mul_i32 s98, s98, s55
	s_add_u32 s98, s64, s98
	s_addc_u32 s99, s65, 0
	global_store_dwordx4 v6, v[104:107], s[98:99] nt
	s_movk_i32 s98, 112
	s_mul_i32 s98, s98, s55
	s_add_u32 s98, s64, s98
	s_addc_u32 s99, s65, 0
	global_store_dwordx4 v6, v[108:111], s[98:99] nt
	s_add_i32 s98, s83, 32
	s_and_b32 s98, s98, 31
	v_xor_b32_e32 v7, s98, v14
	v_lshlrev_b32_e32 v7, 4, v7
	s_mov_b32 s99, 65536
	v_add3_u32 v7, v7, v18, s99
	ds_read_b128 v[96:99], v7
	s_add_i32 s98, s83, 36
	s_and_b32 s98, s98, 31
	v_xor_b32_e32 v7, s98, v14
	v_lshlrev_b32_e32 v7, 4, v7
	s_mov_b32 s99, 73728
	v_add3_u32 v7, v7, v18, s99
	ds_read_b128 v[100:103], v7
	s_add_i32 s98, s83, 40
	s_and_b32 s98, s98, 31
	v_xor_b32_e32 v7, s98, v14
	v_lshlrev_b32_e32 v7, 4, v7
	s_mov_b32 s99, 81920
	v_add3_u32 v7, v7, v18, s99
	ds_read_b128 v[104:107], v7
	s_add_i32 s98, s83, 44
	s_and_b32 s98, s98, 31
	v_xor_b32_e32 v7, s98, v14
	v_lshlrev_b32_e32 v7, 4, v7
	s_mov_b32 s99, 90112
	v_add3_u32 v7, v7, v18, s99
	ds_read_b128 v[108:111], v7
	s_waitcnt lgkmcnt(0)
	s_movk_i32 s98, 128
	s_cmp_eq_u32 s67, 1
	s_cselect_b32 s98, 256, s98
	s_mul_i32 s98, s98, s55
	s_add_u32 s98, s64, s98
	s_addc_u32 s99, s65, 0
	global_store_dwordx4 v6, v[96:99], s[98:99] nt
	s_movk_i32 s98, 144
	s_cmp_eq_u32 s67, 1
	s_cselect_b32 s98, 272, s98
	s_mul_i32 s98, s98, s55
	s_add_u32 s98, s64, s98
	s_addc_u32 s99, s65, 0
	global_store_dwordx4 v6, v[100:103], s[98:99] nt
	s_movk_i32 s98, 160
	s_cmp_eq_u32 s67, 1
	s_cselect_b32 s98, 288, s98
	s_mul_i32 s98, s98, s55
	s_add_u32 s98, s64, s98
	s_addc_u32 s99, s65, 0
	global_store_dwordx4 v6, v[104:107], s[98:99] nt
	s_movk_i32 s98, 176
	s_cmp_eq_u32 s67, 1
	s_cselect_b32 s98, 304, s98
	s_mul_i32 s98, s98, s55
	s_add_u32 s98, s64, s98
	s_addc_u32 s99, s65, 0
	global_store_dwordx4 v6, v[108:111], s[98:99] nt
	s_add_i32 s98, s83, 48
	s_and_b32 s98, s98, 31
	v_xor_b32_e32 v7, s98, v14
	v_lshlrev_b32_e32 v7, 4, v7
	s_mov_b32 s99, 98304
	v_add3_u32 v7, v7, v18, s99
	ds_read_b128 v[96:99], v7
	s_add_i32 s98, s83, 52
	s_and_b32 s98, s98, 31
	v_xor_b32_e32 v7, s98, v14
	v_lshlrev_b32_e32 v7, 4, v7
	s_mov_b32 s99, 106496
	v_add3_u32 v7, v7, v18, s99
	ds_read_b128 v[100:103], v7
	s_add_i32 s98, s83, 56
	s_and_b32 s98, s98, 31
	v_xor_b32_e32 v7, s98, v14
	v_lshlrev_b32_e32 v7, 4, v7
	s_mov_b32 s99, 114688
	v_add3_u32 v7, v7, v18, s99
	ds_read_b128 v[104:107], v7
	s_add_i32 s98, s83, 60
	s_and_b32 s98, s98, 31
	v_xor_b32_e32 v7, s98, v14
	v_lshlrev_b32_e32 v7, 4, v7
	s_mov_b32 s99, 122880
	v_add3_u32 v7, v7, v18, s99
	ds_read_b128 v[108:111], v7
	s_waitcnt lgkmcnt(0)
	s_movk_i32 s98, 192
	s_cmp_eq_u32 s67, 1
	s_cselect_b32 s98, 320, s98
	s_mul_i32 s98, s98, s55
	s_add_u32 s98, s64, s98
	s_addc_u32 s99, s65, 0
	global_store_dwordx4 v6, v[96:99], s[98:99] nt
	s_movk_i32 s98, 208
	s_cmp_eq_u32 s67, 1
	s_cselect_b32 s98, 336, s98
	s_mul_i32 s98, s98, s55
	s_add_u32 s98, s64, s98
	s_addc_u32 s99, s65, 0
	global_store_dwordx4 v6, v[100:103], s[98:99] nt
	s_movk_i32 s98, 224
	s_cmp_eq_u32 s67, 1
	s_cselect_b32 s98, 352, s98
	s_mul_i32 s98, s98, s55
	s_add_u32 s98, s64, s98
	s_addc_u32 s99, s65, 0
	global_store_dwordx4 v6, v[104:107], s[98:99] nt
	s_movk_i32 s98, 240
	s_cmp_eq_u32 s67, 1
	s_cselect_b32 s98, 368, s98
	s_mul_i32 s98, s98, s55
	s_add_u32 s98, s64, s98
	s_addc_u32 s99, s65, 0
	global_store_dwordx4 v6, v[108:111], s[98:99] nt
	s_bitcmp1_b32 s100, 24
	s_cbranch_scc1 .Lcv_spinc
	s_add_i32 s101, s101, 1
	s_branch .Lcv_cnt
